# v16 + nt on the P12 expert-output (Y) row gathers only (full-line, read once)
# speedup vs baseline: 1.0150x; 1.0150x over previous
.LBB0_2063:
	s_ashr_i32 s7, s6, 31
	s_lshl_b64 s[10:11], s[6:7], 2
	s_add_u32 s10, s9, s10
	s_addc_u32 s11, s12, s11
	global_load_dwordx4 v[0:3], v37, s[10:11]
	global_load_dwordx4 v[4:7], v37, s[10:11] offset:16
	s_add_i32 s14, s0, 0x14000
	s_ashr_i32 s15, s14, 31
	s_lshl_b64 s[10:11], s[14:15], 11
	v_lshl_add_u64 v[76:77], v[38:39], 0, s[10:11]
	s_add_i32 s0, s0, s2
	s_add_i32 s6, s6, s1
	s_cmpk_lt_i32 s0, 0x2000
	s_waitcnt vmcnt(1)
	v_ashrrev_i32_e32 v9, 31, v0
	v_mov_b32_e32 v8, v0
	v_ashrrev_i32_e32 v11, 31, v1
	v_mov_b32_e32 v10, v1
	v_ashrrev_i32_e32 v1, 31, v2
	v_mov_b32_e32 v0, v2
	v_ashrrev_i32_e32 v13, 31, v3
	v_mov_b32_e32 v12, v3
	s_waitcnt vmcnt(0)
	v_ashrrev_i32_e32 v3, 31, v4
	v_mov_b32_e32 v2, v4
	v_ashrrev_i32_e32 v15, 31, v5
	v_mov_b32_e32 v14, v5
	v_ashrrev_i32_e32 v5, 31, v6
	v_mov_b32_e32 v4, v6
	v_ashrrev_i32_e32 v17, 31, v7
	v_mov_b32_e32 v16, v7
	v_lshlrev_b64 v[56:57], 11, v[8:9]
	v_lshlrev_b64 v[48:49], 11, v[10:11]
	v_lshlrev_b64 v[50:51], 11, v[12:13]
	v_lshlrev_b64 v[58:59], 11, v[0:1]
	v_lshlrev_b64 v[52:53], 11, v[14:15]
	v_lshlrev_b64 v[60:61], 11, v[2:3]
	v_lshlrev_b64 v[54:55], 11, v[16:17]
	v_lshlrev_b64 v[62:63], 11, v[4:5]
	v_lshl_add_u64 v[78:79], v[38:39], 0, v[56:57]
	v_lshl_add_u64 v[80:81], v[38:39], 0, v[48:49]
	v_lshl_add_u64 v[82:83], v[38:39], 0, v[58:59]
	v_lshl_add_u64 v[84:85], v[38:39], 0, v[50:51]
	v_lshl_add_u64 v[86:87], v[38:39], 0, v[60:61]
	v_lshl_add_u64 v[88:89], v[38:39], 0, v[52:53]
	v_lshl_add_u64 v[90:91], v[38:39], 0, v[62:63]
	v_lshl_add_u64 v[92:93], v[38:39], 0, v[54:55]
	global_load_dwordx4 v[32:35], v[78:79], off nt
	global_load_dwordx4 v[28:31], v[80:81], off nt
	global_load_dwordx4 v[24:27], v[82:83], off nt
	global_load_dwordx4 v[20:23], v[84:85], off nt
	global_load_dwordx4 v[16:19], v[86:87], off nt
	global_load_dwordx4 v[12:15], v[88:89], off nt
	global_load_dwordx4 v[8:11], v[90:91], off nt
	global_load_dwordx4 v[4:7], v[92:93], off nt
	global_load_dwordx4 v[0:3], v[76:77], off nt
	global_load_dwordx4 v[64:67], v[40:41], off
	global_load_dwordx4 v[68:71], v[46:47], off offset:-4096
	global_load_dwordx4 v[72:75], v[46:47], off offset:-4080
	v_lshl_add_u64 v[60:61], v[44:45], 0, v[60:61]
	v_lshl_add_u64 v[62:63], v[44:45], 0, v[62:63]
	s_waitcnt vmcnt(11)
	v_cvt_pk_f32_fp8_e32 v[76:77], v32
	v_cvt_pk_f32_fp8_sdwa v[78:79], v32 src0_sel:WORD_1
	s_waitcnt vmcnt(10)
	v_cvt_pk_f32_fp8_e32 v[80:81], v28
	v_cvt_pk_f32_fp8_sdwa v[82:83], v28 src0_sel:WORD_1
	s_waitcnt vmcnt(9)
	v_cvt_pk_f32_fp8_e32 v[84:85], v24
	v_cvt_pk_f32_fp8_sdwa v[86:87], v24 src0_sel:WORD_1
	s_waitcnt vmcnt(8)
	v_cvt_pk_f32_fp8_e32 v[88:89], v20
	v_cvt_pk_f32_fp8_sdwa v[90:91], v20 src0_sel:WORD_1
	s_waitcnt vmcnt(7)
	v_cvt_pk_f32_fp8_e32 v[92:93], v16
	v_cvt_pk_f32_fp8_sdwa v[94:95], v16 src0_sel:WORD_1
	v_pk_add_f32 v[76:77], v[76:77], 0 op_sel_hi:[1,0]
	v_pk_add_f32 v[78:79], v[78:79], 0 op_sel_hi:[1,0]
	s_waitcnt vmcnt(6)
	v_cvt_pk_f32_fp8_e32 v[96:97], v12
	v_cvt_pk_f32_fp8_sdwa v[98:99], v12 src0_sel:WORD_1
	v_pk_add_f32 v[78:79], v[78:79], v[82:83]
	v_pk_add_f32 v[76:77], v[76:77], v[80:81]
	s_waitcnt vmcnt(5)
	v_cvt_pk_f32_fp8_e32 v[100:101], v8
	v_cvt_pk_f32_fp8_sdwa v[102:103], v8 src0_sel:WORD_1
	v_pk_add_f32 v[76:77], v[76:77], v[84:85]
	v_pk_add_f32 v[78:79], v[78:79], v[86:87]
	s_waitcnt vmcnt(4)
	v_cvt_pk_f32_fp8_e32 v[104:105], v4
	v_cvt_pk_f32_fp8_sdwa v[106:107], v4 src0_sel:WORD_1
	v_pk_add_f32 v[78:79], v[78:79], v[90:91]
	v_pk_add_f32 v[76:77], v[76:77], v[88:89]
	s_waitcnt vmcnt(3)
	v_cvt_pk_f32_fp8_e32 v[108:109], v0
	v_cvt_pk_f32_fp8_sdwa v[110:111], v0 src0_sel:WORD_1
	v_pk_add_f32 v[76:77], v[76:77], v[92:93]
	v_pk_add_f32 v[78:79], v[78:79], v[94:95]
	v_pk_add_f32 v[76:77], v[76:77], v[96:97]
	v_pk_add_f32 v[78:79], v[78:79], v[98:99]
	v_pk_add_f32 v[76:77], v[76:77], v[100:101]
	v_pk_add_f32 v[78:79], v[78:79], v[102:103]
	v_pk_add_f32 v[76:77], v[76:77], v[104:105]
	v_pk_add_f32 v[78:79], v[78:79], v[106:107]
	s_waitcnt vmcnt(2)
	v_pk_mul_f32 v[66:67], v[66:67], s[8:9] op_sel_hi:[1,0]
	v_pk_mul_f32 v[64:65], v[64:65], s[8:9] op_sel_hi:[1,0]
	v_pk_add_f32 v[76:77], v[76:77], v[108:109]
	v_pk_add_f32 v[78:79], v[78:79], v[110:111]
	s_waitcnt vmcnt(1)
	v_pk_fma_f32 v[64:65], v[76:77], v[64:65], v[68:69]
	v_pk_fma_f32 v[66:67], v[78:79], v[66:67], v[70:71]
	global_store_dwordx4 v[46:47], v[64:67], off offset:-4096
	global_load_dwordx4 v[64:67], v[40:41], off offset:16
	v_cvt_pk_f32_fp8_e32 v[68:69], v33
	v_cvt_pk_f32_fp8_sdwa v[32:33], v33 src0_sel:WORD_1
	v_cvt_pk_f32_fp8_e32 v[70:71], v29
	v_cvt_pk_f32_fp8_sdwa v[28:29], v29 src0_sel:WORD_1
	v_cvt_pk_f32_fp8_e32 v[76:77], v25
	v_cvt_pk_f32_fp8_sdwa v[24:25], v25 src0_sel:WORD_1
	v_cvt_pk_f32_fp8_e32 v[78:79], v21
	v_cvt_pk_f32_fp8_sdwa v[20:21], v21 src0_sel:WORD_1
	v_cvt_pk_f32_fp8_e32 v[80:81], v17
	v_cvt_pk_f32_fp8_sdwa v[16:17], v17 src0_sel:WORD_1
	v_pk_add_f32 v[32:33], v[32:33], 0 op_sel_hi:[1,0]
	v_pk_add_f32 v[68:69], v[68:69], 0 op_sel_hi:[1,0]
	v_cvt_pk_f32_fp8_e32 v[82:83], v13
	v_cvt_pk_f32_fp8_sdwa v[12:13], v13 src0_sel:WORD_1
	v_pk_add_f32 v[68:69], v[68:69], v[70:71]
	v_pk_add_f32 v[28:29], v[32:33], v[28:29]
	v_cvt_pk_f32_fp8_e32 v[84:85], v9
	v_cvt_pk_f32_fp8_sdwa v[8:9], v9 src0_sel:WORD_1
	v_pk_add_f32 v[24:25], v[28:29], v[24:25]
	v_pk_add_f32 v[28:29], v[68:69], v[76:77]
	v_cvt_pk_f32_fp8_e32 v[86:87], v5
	v_cvt_pk_f32_fp8_sdwa v[4:5], v5 src0_sel:WORD_1
	v_pk_add_f32 v[28:29], v[28:29], v[78:79]
	v_pk_add_f32 v[20:21], v[24:25], v[20:21]
	v_cvt_pk_f32_fp8_e32 v[88:89], v1
	v_cvt_pk_f32_fp8_sdwa v[0:1], v1 src0_sel:WORD_1
	v_pk_add_f32 v[16:17], v[20:21], v[16:17]
	v_pk_add_f32 v[20:21], v[28:29], v[80:81]
	v_pk_add_f32 v[12:13], v[16:17], v[12:13]
	v_pk_add_f32 v[20:21], v[20:21], v[82:83]
	v_pk_add_f32 v[8:9], v[12:13], v[8:9]
	v_pk_add_f32 v[12:13], v[20:21], v[84:85]
	v_pk_add_f32 v[4:5], v[8:9], v[4:5]
	v_pk_add_f32 v[12:13], v[12:13], v[86:87]
	v_pk_add_f32 v[0:1], v[4:5], v[0:1]
	v_pk_add_f32 v[4:5], v[12:13], v[88:89]
	v_cvt_pk_f32_fp8_e32 v[16:17], v26
	v_cvt_pk_f32_fp8_sdwa v[20:21], v26 src0_sel:WORD_1
	v_cvt_pk_f32_fp8_e32 v[24:25], v22
	v_cvt_pk_f32_fp8_sdwa v[28:29], v22 src0_sel:WORD_1
	v_cvt_pk_f32_fp8_e32 v[32:33], v18
	v_cvt_pk_f32_fp8_sdwa v[78:79], v18 src0_sel:WORD_1
	v_cvt_pk_f32_fp8_e32 v[80:81], v14
	v_cvt_pk_f32_fp8_sdwa v[82:83], v14 src0_sel:WORD_1
	v_cvt_pk_f32_fp8_e32 v[84:85], v10
	v_cvt_pk_f32_fp8_sdwa v[86:87], v10 src0_sel:WORD_1
	v_cvt_pk_f32_fp8_e32 v[88:89], v6
	v_cvt_pk_f32_fp8_sdwa v[90:91], v6 src0_sel:WORD_1
	v_cvt_pk_f32_fp8_e32 v[92:93], v2
	v_cvt_pk_f32_fp8_sdwa v[94:95], v2 src0_sel:WORD_1
	v_lshl_add_u64 v[76:77], v[44:45], 0, s[10:11]
	s_waitcnt vmcnt(0)
	v_pk_mul_f32 v[8:9], v[66:67], s[8:9] op_sel_hi:[1,0]
	v_pk_mul_f32 v[12:13], v[64:65], s[8:9] op_sel_hi:[1,0]
	v_pk_fma_f32 v[66:67], v[0:1], v[8:9], v[74:75]
	v_pk_fma_f32 v[64:65], v[4:5], v[12:13], v[72:73]
	global_store_dwordx4 v[46:47], v[64:67], off offset:-4080
	global_load_dwordx4 v[64:67], v[40:41], off offset:32
	s_nop 0
	global_load_dwordx4 v[68:71], v[46:47], off offset:-4064
	global_load_dwordx4 v[72:75], v[46:47], off offset:-4048
	v_cvt_pk_f32_fp8_e32 v[0:1], v34
	v_cvt_pk_f32_fp8_sdwa v[4:5], v34 src0_sel:WORD_1
	v_cvt_pk_f32_fp8_e32 v[8:9], v30
	v_cvt_pk_f32_fp8_sdwa v[12:13], v30 src0_sel:WORD_1
	v_pk_add_f32 v[0:1], v[0:1], 0 op_sel_hi:[1,0]
	v_pk_add_f32 v[4:5], v[4:5], 0 op_sel_hi:[1,0]
	v_pk_add_f32 v[0:1], v[0:1], v[8:9]
	v_pk_add_f32 v[4:5], v[4:5], v[12:13]
	v_pk_add_f32 v[0:1], v[0:1], v[16:17]
	v_pk_add_f32 v[4:5], v[4:5], v[20:21]
	v_pk_add_f32 v[0:1], v[0:1], v[24:25]
	v_pk_add_f32 v[4:5], v[4:5], v[28:29]
	v_pk_add_f32 v[0:1], v[0:1], v[32:33]
	v_pk_add_f32 v[4:5], v[4:5], v[78:79]
	v_pk_add_f32 v[0:1], v[0:1], v[80:81]
	v_pk_add_f32 v[4:5], v[4:5], v[82:83]
	v_pk_add_f32 v[0:1], v[0:1], v[84:85]
	v_pk_add_f32 v[4:5], v[4:5], v[86:87]
	v_pk_add_f32 v[0:1], v[0:1], v[88:89]
	v_pk_add_f32 v[4:5], v[4:5], v[90:91]
	v_pk_add_f32 v[0:1], v[0:1], v[92:93]
	v_pk_add_f32 v[4:5], v[4:5], v[94:95]
	v_cvt_pk_f32_fp8_e32 v[16:17], v27
	v_cvt_pk_f32_fp8_sdwa v[20:21], v27 src0_sel:WORD_1
	v_cvt_pk_f32_fp8_e32 v[24:25], v23
	v_cvt_pk_f32_fp8_sdwa v[22:23], v23 src0_sel:WORD_1
	v_cvt_pk_f32_fp8_e32 v[26:27], v19
	v_cvt_pk_f32_fp8_sdwa v[18:19], v19 src0_sel:WORD_1
	v_cvt_pk_f32_fp8_e32 v[28:29], v15
	v_cvt_pk_f32_fp8_sdwa v[14:15], v15 src0_sel:WORD_1
	v_cvt_pk_f32_fp8_e32 v[32:33], v7
	v_cvt_pk_f32_fp8_sdwa v[6:7], v7 src0_sel:WORD_1
	v_lshl_add_u64 v[78:79], v[44:45], 0, v[58:59]
	v_lshl_add_u64 v[80:81], v[44:45], 0, v[50:51]
	v_lshl_add_u64 v[82:83], v[44:45], 0, v[52:53]
	v_lshl_add_u64 v[84:85], v[44:45], 0, v[54:55]
	s_waitcnt vmcnt(2)
	v_pk_mul_f32 v[8:9], v[66:67], s[8:9] op_sel_hi:[1,0]
	v_pk_mul_f32 v[12:13], v[64:65], s[8:9] op_sel_hi:[1,0]
	s_waitcnt vmcnt(1)
	v_pk_fma_f32 v[66:67], v[4:5], v[8:9], v[70:71]
	v_pk_fma_f32 v[64:65], v[0:1], v[12:13], v[68:69]
	global_store_dwordx4 v[46:47], v[64:67], off offset:-4064
	global_load_dwordx4 v[64:67], v[40:41], off offset:48
	v_cvt_pk_f32_fp8_e32 v[0:1], v35
	v_cvt_pk_f32_fp8_sdwa v[4:5], v35 src0_sel:WORD_1
	v_cvt_pk_f32_fp8_e32 v[8:9], v31
	v_cvt_pk_f32_fp8_sdwa v[12:13], v31 src0_sel:WORD_1
	v_pk_add_f32 v[0:1], v[0:1], 0 op_sel_hi:[1,0]
	v_pk_add_f32 v[4:5], v[4:5], 0 op_sel_hi:[1,0]
	v_pk_add_f32 v[0:1], v[0:1], v[8:9]
	v_pk_add_f32 v[4:5], v[4:5], v[12:13]
	v_cvt_pk_f32_fp8_e32 v[30:31], v11
	v_cvt_pk_f32_fp8_sdwa v[10:11], v11 src0_sel:WORD_1
	v_pk_add_f32 v[4:5], v[4:5], v[20:21]
	v_pk_add_f32 v[0:1], v[0:1], v[16:17]
	v_pk_add_f32 v[4:5], v[4:5], v[22:23]
	v_pk_add_f32 v[0:1], v[0:1], v[24:25]
	v_cvt_pk_f32_fp8_e32 v[34:35], v3
	v_cvt_pk_f32_fp8_sdwa v[2:3], v3 src0_sel:WORD_1
	v_pk_add_f32 v[4:5], v[4:5], v[18:19]
	v_pk_add_f32 v[0:1], v[0:1], v[26:27]
	v_pk_add_f32 v[4:5], v[4:5], v[14:15]
	v_pk_add_f32 v[0:1], v[0:1], v[28:29]
	v_pk_add_f32 v[4:5], v[4:5], v[10:11]
	v_pk_add_f32 v[0:1], v[0:1], v[30:31]
	v_pk_add_f32 v[4:5], v[4:5], v[6:7]
	v_pk_add_f32 v[0:1], v[0:1], v[32:33]
	v_pk_add_f32 v[2:3], v[4:5], v[2:3]
	v_pk_add_f32 v[0:1], v[0:1], v[34:35]
	v_lshl_add_u64 v[68:69], v[44:45], 0, v[56:57]
	v_lshl_add_u64 v[70:71], v[44:45], 0, v[48:49]
	s_waitcnt vmcnt(0)
	v_pk_mul_f32 v[4:5], v[66:67], s[8:9] op_sel_hi:[1,0]
	v_pk_mul_f32 v[6:7], v[64:65], s[8:9] op_sel_hi:[1,0]
	v_pk_fma_f32 v[2:3], v[2:3], v[4:5], v[74:75]
	v_pk_fma_f32 v[0:1], v[0:1], v[6:7], v[72:73]
	global_store_dwordx4 v[46:47], v[0:3], off offset:-4048
	global_load_dwordx4 v[32:35], v[68:69], off nt
	global_load_dwordx4 v[28:31], v[70:71], off nt
	global_load_dwordx4 v[24:27], v[78:79], off nt
	global_load_dwordx4 v[20:23], v[80:81], off nt
	global_load_dwordx4 v[16:19], v[60:61], off nt
	global_load_dwordx4 v[12:15], v[82:83], off nt
	global_load_dwordx4 v[8:11], v[62:63], off nt
	global_load_dwordx4 v[4:7], v[84:85], off nt
	global_load_dwordx4 v[0:3], v[76:77], off nt
	global_load_dwordx4 v[48:51], v[42:43], off
	global_load_dwordx4 v[52:55], v[46:47], off
	global_load_dwordx4 v[56:59], v[46:47], off offset:16
	s_waitcnt vmcnt(11)
	v_cvt_pk_f32_fp8_e32 v[60:61], v32
	v_cvt_pk_f32_fp8_sdwa v[62:63], v32 src0_sel:WORD_1
	s_waitcnt vmcnt(10)
	v_cvt_pk_f32_fp8_e32 v[64:65], v28
	v_cvt_pk_f32_fp8_sdwa v[66:67], v28 src0_sel:WORD_1
	s_waitcnt vmcnt(9)
	v_cvt_pk_f32_fp8_e32 v[68:69], v24
	v_cvt_pk_f32_fp8_sdwa v[70:71], v24 src0_sel:WORD_1
	s_waitcnt vmcnt(8)
	v_cvt_pk_f32_fp8_e32 v[72:73], v20
	v_cvt_pk_f32_fp8_sdwa v[74:75], v20 src0_sel:WORD_1
	s_waitcnt vmcnt(7)
	v_cvt_pk_f32_fp8_e32 v[76:77], v16
	v_cvt_pk_f32_fp8_sdwa v[78:79], v16 src0_sel:WORD_1
	v_pk_add_f32 v[60:61], v[60:61], 0 op_sel_hi:[1,0]
	v_pk_add_f32 v[62:63], v[62:63], 0 op_sel_hi:[1,0]
	s_waitcnt vmcnt(6)
	v_cvt_pk_f32_fp8_e32 v[80:81], v12
	v_cvt_pk_f32_fp8_sdwa v[82:83], v12 src0_sel:WORD_1
	v_pk_add_f32 v[62:63], v[62:63], v[66:67]
	v_pk_add_f32 v[60:61], v[60:61], v[64:65]
	s_waitcnt vmcnt(5)
	v_cvt_pk_f32_fp8_e32 v[84:85], v8
	v_cvt_pk_f32_fp8_sdwa v[86:87], v8 src0_sel:WORD_1
	v_pk_add_f32 v[60:61], v[60:61], v[68:69]
	v_pk_add_f32 v[62:63], v[62:63], v[70:71]
	s_waitcnt vmcnt(4)
	v_cvt_pk_f32_fp8_e32 v[88:89], v4
	v_cvt_pk_f32_fp8_sdwa v[90:91], v4 src0_sel:WORD_1
	v_pk_add_f32 v[62:63], v[62:63], v[74:75]
	v_pk_add_f32 v[60:61], v[60:61], v[72:73]
	s_waitcnt vmcnt(3)
	v_cvt_pk_f32_fp8_e32 v[92:93], v0
	v_cvt_pk_f32_fp8_sdwa v[94:95], v0 src0_sel:WORD_1
	v_pk_add_f32 v[60:61], v[60:61], v[76:77]
	v_pk_add_f32 v[62:63], v[62:63], v[78:79]
	v_pk_add_f32 v[60:61], v[60:61], v[80:81]
	v_pk_add_f32 v[62:63], v[62:63], v[82:83]
	v_pk_add_f32 v[60:61], v[60:61], v[84:85]
	v_pk_add_f32 v[62:63], v[62:63], v[86:87]
	v_pk_add_f32 v[60:61], v[60:61], v[88:89]
	v_pk_add_f32 v[62:63], v[62:63], v[90:91]
	s_waitcnt vmcnt(2)
	v_pk_mul_f32 v[50:51], v[50:51], s[8:9] op_sel_hi:[1,0]
	v_pk_mul_f32 v[48:49], v[48:49], s[8:9] op_sel_hi:[1,0]
	v_pk_add_f32 v[60:61], v[60:61], v[92:93]
	v_pk_add_f32 v[62:63], v[62:63], v[94:95]
	s_waitcnt vmcnt(1)
	v_pk_fma_f32 v[48:49], v[60:61], v[48:49], v[52:53]
	v_pk_fma_f32 v[50:51], v[62:63], v[50:51], v[54:55]
	global_store_dwordx4 v[46:47], v[48:51], off
	global_load_dwordx4 v[48:51], v[42:43], off offset:16
	v_cvt_pk_f32_fp8_e32 v[52:53], v33
	v_cvt_pk_f32_fp8_sdwa v[32:33], v33 src0_sel:WORD_1
	v_cvt_pk_f32_fp8_e32 v[54:55], v29
	v_cvt_pk_f32_fp8_sdwa v[28:29], v29 src0_sel:WORD_1
	v_cvt_pk_f32_fp8_e32 v[60:61], v25
	v_cvt_pk_f32_fp8_sdwa v[24:25], v25 src0_sel:WORD_1
	v_cvt_pk_f32_fp8_e32 v[62:63], v21
	v_cvt_pk_f32_fp8_sdwa v[20:21], v21 src0_sel:WORD_1
	v_cvt_pk_f32_fp8_e32 v[64:65], v17
	v_cvt_pk_f32_fp8_sdwa v[16:17], v17 src0_sel:WORD_1
	v_pk_add_f32 v[32:33], v[32:33], 0 op_sel_hi:[1,0]
	v_pk_add_f32 v[52:53], v[52:53], 0 op_sel_hi:[1,0]
	v_cvt_pk_f32_fp8_e32 v[66:67], v13
	v_cvt_pk_f32_fp8_sdwa v[12:13], v13 src0_sel:WORD_1
	v_pk_add_f32 v[52:53], v[52:53], v[54:55]
	v_pk_add_f32 v[28:29], v[32:33], v[28:29]
	v_cvt_pk_f32_fp8_e32 v[68:69], v9
	v_cvt_pk_f32_fp8_sdwa v[8:9], v9 src0_sel:WORD_1
	v_pk_add_f32 v[24:25], v[28:29], v[24:25]
	v_pk_add_f32 v[28:29], v[52:53], v[60:61]
	v_cvt_pk_f32_fp8_e32 v[70:71], v5
	v_cvt_pk_f32_fp8_sdwa v[4:5], v5 src0_sel:WORD_1
	v_pk_add_f32 v[28:29], v[28:29], v[62:63]
	v_pk_add_f32 v[20:21], v[24:25], v[20:21]
	v_cvt_pk_f32_fp8_e32 v[72:73], v1
	v_cvt_pk_f32_fp8_sdwa v[0:1], v1 src0_sel:WORD_1
	v_pk_add_f32 v[16:17], v[20:21], v[16:17]
	v_pk_add_f32 v[20:21], v[28:29], v[64:65]
	v_pk_add_f32 v[12:13], v[16:17], v[12:13]
	v_pk_add_f32 v[20:21], v[20:21], v[66:67]
	v_pk_add_f32 v[8:9], v[12:13], v[8:9]
	v_pk_add_f32 v[12:13], v[20:21], v[68:69]
	v_pk_add_f32 v[4:5], v[8:9], v[4:5]
	v_pk_add_f32 v[12:13], v[12:13], v[70:71]
	v_pk_add_f32 v[0:1], v[4:5], v[0:1]
	v_pk_add_f32 v[4:5], v[12:13], v[72:73]
	v_cvt_pk_f32_fp8_e32 v[16:17], v26
	v_cvt_pk_f32_fp8_sdwa v[20:21], v26 src0_sel:WORD_1
	v_cvt_pk_f32_fp8_e32 v[24:25], v22
	v_cvt_pk_f32_fp8_sdwa v[28:29], v22 src0_sel:WORD_1
	v_cvt_pk_f32_fp8_e32 v[32:33], v18
	v_cvt_pk_f32_fp8_sdwa v[60:61], v18 src0_sel:WORD_1
	v_cvt_pk_f32_fp8_e32 v[62:63], v14
	v_cvt_pk_f32_fp8_sdwa v[64:65], v14 src0_sel:WORD_1
	v_cvt_pk_f32_fp8_e32 v[66:67], v10
	v_cvt_pk_f32_fp8_sdwa v[68:69], v10 src0_sel:WORD_1
	v_cvt_pk_f32_fp8_e32 v[70:71], v6
	v_cvt_pk_f32_fp8_sdwa v[72:73], v6 src0_sel:WORD_1
	v_cvt_pk_f32_fp8_e32 v[74:75], v2
	v_cvt_pk_f32_fp8_sdwa v[76:77], v2 src0_sel:WORD_1
	s_waitcnt vmcnt(0)
	v_pk_mul_f32 v[8:9], v[50:51], s[8:9] op_sel_hi:[1,0]
	v_pk_mul_f32 v[12:13], v[48:49], s[8:9] op_sel_hi:[1,0]
	v_pk_fma_f32 v[50:51], v[0:1], v[8:9], v[58:59]
	v_pk_fma_f32 v[48:49], v[4:5], v[12:13], v[56:57]
	global_store_dwordx4 v[46:47], v[48:51], off offset:16
	global_load_dwordx4 v[48:51], v[42:43], off offset:32
	s_nop 0
	global_load_dwordx4 v[52:55], v[46:47], off offset:32
	global_load_dwordx4 v[56:59], v[46:47], off offset:48
	v_cvt_pk_f32_fp8_e32 v[0:1], v34
	v_cvt_pk_f32_fp8_sdwa v[4:5], v34 src0_sel:WORD_1
	v_cvt_pk_f32_fp8_e32 v[8:9], v30
	v_cvt_pk_f32_fp8_sdwa v[12:13], v30 src0_sel:WORD_1
	v_pk_add_f32 v[0:1], v[0:1], 0 op_sel_hi:[1,0]
	v_pk_add_f32 v[4:5], v[4:5], 0 op_sel_hi:[1,0]
	v_pk_add_f32 v[0:1], v[0:1], v[8:9]
	v_pk_add_f32 v[4:5], v[4:5], v[12:13]
	v_pk_add_f32 v[0:1], v[0:1], v[16:17]
	v_pk_add_f32 v[4:5], v[4:5], v[20:21]
	v_pk_add_f32 v[0:1], v[0:1], v[24:25]
	v_pk_add_f32 v[4:5], v[4:5], v[28:29]
	v_pk_add_f32 v[0:1], v[0:1], v[32:33]
	v_pk_add_f32 v[4:5], v[4:5], v[60:61]
	v_pk_add_f32 v[0:1], v[0:1], v[62:63]
	v_pk_add_f32 v[4:5], v[4:5], v[64:65]
	v_pk_add_f32 v[0:1], v[0:1], v[66:67]
	v_pk_add_f32 v[4:5], v[4:5], v[68:69]
	v_pk_add_f32 v[0:1], v[0:1], v[70:71]
	v_pk_add_f32 v[4:5], v[4:5], v[72:73]
	v_pk_add_f32 v[0:1], v[0:1], v[74:75]
	v_pk_add_f32 v[4:5], v[4:5], v[76:77]
	v_cvt_pk_f32_fp8_e32 v[16:17], v27
	v_cvt_pk_f32_fp8_sdwa v[20:21], v27 src0_sel:WORD_1
	v_cvt_pk_f32_fp8_e32 v[24:25], v23
	v_cvt_pk_f32_fp8_sdwa v[22:23], v23 src0_sel:WORD_1
	v_cvt_pk_f32_fp8_e32 v[26:27], v19
	v_cvt_pk_f32_fp8_sdwa v[18:19], v19 src0_sel:WORD_1
	v_cvt_pk_f32_fp8_e32 v[28:29], v15
	v_cvt_pk_f32_fp8_sdwa v[14:15], v15 src0_sel:WORD_1
	v_cvt_pk_f32_fp8_e32 v[32:33], v7
	v_cvt_pk_f32_fp8_sdwa v[6:7], v7 src0_sel:WORD_1
	s_waitcnt vmcnt(2)
	v_pk_mul_f32 v[8:9], v[50:51], s[8:9] op_sel_hi:[1,0]
	v_pk_mul_f32 v[12:13], v[48:49], s[8:9] op_sel_hi:[1,0]
	s_waitcnt vmcnt(1)
	v_pk_fma_f32 v[50:51], v[4:5], v[8:9], v[54:55]
	v_pk_fma_f32 v[48:49], v[0:1], v[12:13], v[52:53]
	global_store_dwordx4 v[46:47], v[48:51], off offset:32
	global_load_dwordx4 v[48:51], v[42:43], off offset:48
	v_cvt_pk_f32_fp8_e32 v[0:1], v35
	v_cvt_pk_f32_fp8_sdwa v[4:5], v35 src0_sel:WORD_1
	v_cvt_pk_f32_fp8_e32 v[8:9], v31
	v_cvt_pk_f32_fp8_sdwa v[12:13], v31 src0_sel:WORD_1
	v_pk_add_f32 v[0:1], v[0:1], 0 op_sel_hi:[1,0]
	v_pk_add_f32 v[4:5], v[4:5], 0 op_sel_hi:[1,0]
	v_pk_add_f32 v[0:1], v[0:1], v[8:9]
	v_pk_add_f32 v[4:5], v[4:5], v[12:13]
	v_cvt_pk_f32_fp8_e32 v[30:31], v11
	v_cvt_pk_f32_fp8_sdwa v[10:11], v11 src0_sel:WORD_1
	v_pk_add_f32 v[4:5], v[4:5], v[20:21]
	v_pk_add_f32 v[0:1], v[0:1], v[16:17]
	v_pk_add_f32 v[4:5], v[4:5], v[22:23]
	v_pk_add_f32 v[0:1], v[0:1], v[24:25]
	v_cvt_pk_f32_fp8_e32 v[34:35], v3
	v_cvt_pk_f32_fp8_sdwa v[2:3], v3 src0_sel:WORD_1
	v_pk_add_f32 v[4:5], v[4:5], v[18:19]
	v_pk_add_f32 v[0:1], v[0:1], v[26:27]
	v_pk_add_f32 v[4:5], v[4:5], v[14:15]
	v_pk_add_f32 v[0:1], v[0:1], v[28:29]
	v_pk_add_f32 v[4:5], v[4:5], v[10:11]
	v_pk_add_f32 v[0:1], v[0:1], v[30:31]
	v_pk_add_f32 v[4:5], v[4:5], v[6:7]
	v_pk_add_f32 v[0:1], v[0:1], v[32:33]
	v_pk_add_f32 v[2:3], v[4:5], v[2:3]
	v_pk_add_f32 v[0:1], v[0:1], v[34:35]
	s_waitcnt vmcnt(0)
	v_pk_mul_f32 v[4:5], v[50:51], s[8:9] op_sel_hi:[1,0]
	v_pk_mul_f32 v[6:7], v[48:49], s[8:9] op_sel_hi:[1,0]
	v_pk_fma_f32 v[2:3], v[2:3], v[4:5], v[58:59]
	v_pk_fma_f32 v[0:1], v[0:1], v[6:7], v[56:57]
	global_store_dwordx4 v[46:47], v[0:3], off offset:48
	v_lshl_add_u64 v[46:47], v[46:47], 0, s[4:5]
	s_cbranch_scc1 .LBB0_2063
